# P1: each wave takes 9 consecutive rows (one batch), modulation rows re-loaded only when the batch changes; early L1 invalidate on all barriers
# baseline (speedup 1.0000x reference)
; __device__ __forceinline__ void phase1(const Args& a, int lane, int wave, int vcu, int G) {
;     ...
;     for (int m = vcu * 8 + wave; m < MROWS; m += G * 8) {
;         const float* xr = m < NT ? a.in[0] + (size_t)m * 2048 : a.in[2] + (size_t)(m - NT) * 2048;
;         const float* mr = mod + (size_t)(m < NT ? (m >> 11) : 8) * 12288;
;         f32x4 v[8]; float ss = 0.f;
; #pragma unroll
;         for (int j = 0; j < 8; ++j) { v[j] = __builtin_nontemporal_load((const f32x4*)(xr + 4 * (lane + 64 * j))); ss += v[j][0] * v[j][0] + v[j][1] * v[j][1] + v[j][2] * v[j][2] + v[j][3] * v[j][3]; }
.LBB0_87:
	s_cmp_gt_i32 s94, 1
	s_cselect_b64 s[0:1], -1, 0
	s_cmp_lt_i32 s95, 2
	s_cselect_b64 s[2:3], -1, 0
	s_or_b64 s[0:1], s[0:1], s[2:3]
	s_and_b64 vcc, exec, s[0:1]
	s_cbranch_vccnz .LBB0_143
	v_mov_b32_e32 v1, v0
	s_nop 0
	v_readfirstlane_b32 s0, v1
	s_ashr_i32 s1, s0, 6
	v_readlane_b32 s0, v246, 2
	s_lshl_b32 s2, s0, 3
	s_add_i32 s0, s1, s2
	s_cmpk_gt_i32 s0, 0x47ff
	s_cbranch_scc1 .LBB0_93
	v_lshlrev_b32_e32 v1, 2, v1
	v_and_b32_e32 v2, 0xfc, v1
	v_mov_b32_e32 v5, 0
	v_lshlrev_b32_e32 v4, 2, v2
	v_or_b32_e32 v12, 0x400, v2
	s_waitcnt lgkmcnt(0)
	v_lshl_add_u64 v[26:27], s[80:81], 0, v[4:5]
	v_or_b32_e32 v14, 0x500, v2
	v_lshlrev_b32_e32 v4, 2, v12
	v_or_b32_e32 v16, 0x600, v2
	v_lshl_add_u64 v[28:29], s[80:81], 0, v[4:5]
	v_lshlrev_b32_e32 v4, 2, v14
	v_or_b32_e32 v18, 0x700, v2
	v_lshl_add_u64 v[30:31], s[80:81], 0, v[4:5]
	v_lshlrev_b32_e32 v4, 2, v16
	v_lshl_add_u64 v[32:33], s[80:81], 0, v[4:5]
	v_lshlrev_b32_e32 v4, 2, v18
	v_lshl_add_u64 v[34:35], s[80:81], 0, v[4:5]
	v_lshlrev_b32_e32 v4, 1, v2
	s_add_u32 s16, s92, 0x100000
	v_lshl_add_u64 v[4:5], s[92:93], 0, v[4:5]
	s_mov_b64 s[4:5], 0x1a200000
	s_addc_u32 s17, s93, 0
	s_mov_b32 s0, 1
	v_lshl_add_u64 v[36:37], v[4:5], 0, s[4:5]
	s_ashr_i32 s3, s1, 31
	s_ashr_i32 s5, s2, 31
	s_add_u32 s4, s1, s2
	s_addc_u32 s5, s3, s5
	s_mul_i32 s4, s4, 9
	s_mov_b32 s5, 0
	s_add_i32 s22, s4, 9
	s_mov_b32 s23, -1
	s_ashr_i32 s1, s0, 31
	s_lshl_b64 s[2:3], s[4:5], 13
	v_or_b32_e32 v6, 0x100, v2
	v_or_b32_e32 v8, 0x200, v2
	v_or_b32_e32 v10, 0x300, v2
	s_add_u32 s6, s68, s2
	s_addc_u32 s7, s69, s3
	s_lshl_b64 s[8:9], s[0:1], 13
	s_mov_b32 s11, 0
	v_lshlrev_b32_e32 v1, 2, v2
	v_lshlrev_b32_e32 v41, 2, v12
	v_lshlrev_b32_e32 v42, 2, v14
	v_lshlrev_b32_e32 v43, 2, v16
	v_lshlrev_b32_e32 v44, 2, v18
	v_mov_b32_e32 v45, 0x358637bd
	v_mov_b32_e32 v46, 0x3a000000
	s_mov_b32 s18, 0x800000
	s_movk_i32 s19, 0x7fff
	s_mov_b32 s20, 0xffff0000
	v_lshlrev_b32_e32 v47, 2, v6
	v_lshlrev_b32_e32 v48, 2, v8
	v_lshlrev_b32_e32 v49, 2, v10
	global_load_dwordx4 v[90:93], v[26:27], off
	global_load_dwordx4 v[94:97], v[26:27], off offset:1024
	global_load_dwordx4 v[98:101], v[26:27], off offset:2048
	global_load_dwordx4 v[102:105], v[26:27], off offset:3072
	global_load_dwordx4 v[106:109], v[28:29], off
	global_load_dwordx4 v[110:113], v[30:31], off
	global_load_dwordx4 v[114:117], v[32:33], off
	global_load_dwordx4 v[118:121], v[34:35], off
	s_cmpk_lt_i32 s4, 0x4000
	s_mov_b64 s[12:13], s[6:7]
	s_cbranch_scc1 .Lp1_lat_a
	s_add_i32 s26, s4, 0xffffc000
	s_mov_b32 s27, 0
	s_lshl_b64 s[26:27], s[26:27], 13
	s_add_u32 s12, s72, s26
	s_addc_u32 s13, s73, s27

; __device__ __forceinline__ void phase1(const Args& a, int lane, int wave, int vcu, int G) {
;     ...
;         const float* xr = m < NT ? a.in[0] + (size_t)m * 2048 : a.in[2] + (size_t)(m - NT) * 2048;
;         const float* mr = mod + (size_t)(m < NT ? (m >> 11) : 8) * 12288;
;         f32x4 v[8]; float ss = 0.f;
; #pragma unroll
;         for (int j = 0; j < 8; ++j) { v[j] = __builtin_nontemporal_load((const f32x4*)(xr + 4 * (lane + 64 * j))); ss += v[j][0] * v[j][0] + v[j][1] * v[j][1] + v[j][2] * v[j][2] + v[j][3] * v[j][3]; }
.Lp1_top:
	s_min_i32 s10, s4, 0x4000
	s_ashr_i32 s10, s10, 11
	s_cmp_lg_u32 s10, s23
	s_cselect_b32 s28, 1, 0
	s_mov_b32 s23, s10
	s_cbranch_scc0 .Lp1_nomod_a
	s_mul_hi_i32 s13, s10, 0xc000
	s_mul_i32 s10, s10, 0xc000
	s_add_u32 s12, s16, s10
	s_addc_u32 s13, s17, s13
	s_add_u32 s14, s12, 0x2000
	s_addc_u32 s15, s13, 0
	global_load_dwordx4 v[122:125], v1, s[14:15]
	global_load_dwordx4 v[126:129], v1, s[14:15] offset:1024
	global_load_dwordx4 v[130:133], v1, s[14:15] offset:2048
	global_load_dwordx4 v[134:137], v1, s[14:15] offset:3072
	global_load_dwordx4 v[138:141], v41, s[14:15]
	global_load_dwordx4 v[142:145], v42, s[14:15]
	global_load_dwordx4 v[146:149], v43, s[14:15]
	global_load_dwordx4 v[150:153], v44, s[14:15]
	global_load_dwordx4 v[154:157], v1, s[12:13]
	global_load_dwordx4 v[158:161], v1, s[12:13] offset:1024
	global_load_dwordx4 v[162:165], v1, s[12:13] offset:2048
	global_load_dwordx4 v[166:169], v1, s[12:13] offset:3072
	global_load_dwordx4 v[170:173], v41, s[12:13]
	global_load_dwordx4 v[174:177], v42, s[12:13]
	global_load_dwordx4 v[178:181], v43, s[12:13]
	global_load_dwordx4 v[182:185], v44, s[12:13]
.Lp1_nomod_a:
	v_mov_b32_e32 v40, 0
	v_mov_b32_e32 v84, 0
	s_lshl_b64 s[2:3], s[4:5], 12
	s_add_u32 s4, s4, s0
	s_addc_u32 s5, s5, s1
	s_add_u32 s6, s6, s8
	s_addc_u32 s7, s7, s9
	s_cmp_lt_i32 s4, s22
	s_cselect_b32 s21, 1, 0
	s_cbranch_scc0 .Lp1_last_a
	s_cmpk_lt_i32 s4, 0x4000
	s_mov_b64 s[24:25], s[6:7]
	s_cbranch_scc1 .Lp1_lat_b1
	s_add_i32 s26, s4, 0xffffc000
	s_mov_b32 s27, 0
	s_lshl_b64 s[26:27], s[26:27], 13
	s_add_u32 s24, s72, s26
	s_addc_u32 s25, s73, s27

; __device__ __forceinline__ void phase1(const Args& a, int lane, int wave, int vcu, int G) {
;     ...
;         for (int j = 0; j < 8; ++j) { v[j] = __builtin_nontemporal_load((const f32x4*)(xr + 4 * (lane + 64 * j))); ss += v[j][0] * v[j][0] + v[j][1] * v[j][1] + v[j][2] * v[j][2] + v[j][3] * v[j][3]; }
.Lp1_last_a:
	s_lshl_b32 s29, s28, 1
	s_or_b32 s29, s29, s21
	s_cmp_eq_u32 s29, 3
	s_cbranch_scc1 .Lp1_w24_a
	s_cmp_eq_u32 s29, 2
	s_cbranch_scc1 .Lp1_w16_a
	s_cmp_eq_u32 s29, 1
	s_cbranch_scc1 .Lp1_w8a_a
	s_waitcnt vmcnt(0)
	s_branch .Lp1_red_a
.Lp1_w24_a:
	s_waitcnt vmcnt(24)
	s_branch .Lp1_red_a
.Lp1_w16_a:
	s_waitcnt vmcnt(16)
	s_branch .Lp1_red_a

; __device__ __forceinline__ void phase1(const Args& a, int lane, int wave, int vcu, int G) {
;     ...
;         for (int j = 0; j < 8; ++j) { v[j] = __builtin_nontemporal_load((const f32x4*)(xr + 4 * (lane + 64 * j))); ss += v[j][0] * v[j][0] + v[j][1] * v[j][1] + v[j][2] * v[j][2] + v[j][3] * v[j][3]; }
;         const float rstd = rsqrtf(wave_sum(ss) * (1.f / 2048.f) + EPS);
; #pragma unroll
;         for (int j = 0; j < 8; ++j) { const int c = 4 * (lane + 64 * j); const f32x4 gg = *(const f32x4*)(g + c), sh = *(const f32x4*)(mr + c), sc = *(const f32x4*)(mr + 2048 + c);
;             const f32x4 o = v[j] * rstd * gg * (sc + 1.f) + sh;
.Lp1_red_a:
	v_mul_f32_e32 v85, v50, v50
	v_mul_f32_e32 v86, v54, v54
	v_mul_f32_e32 v87, v22, v22
	v_mul_f32_e32 v88, v18, v18
	v_fmac_f32_e32 v85, v51, v51
	v_fmac_f32_e32 v86, v55, v55
	v_fmac_f32_e32 v87, v23, v23
	v_fmac_f32_e32 v88, v19, v19
	v_fmac_f32_e32 v85, v52, v52
	v_fmac_f32_e32 v86, v56, v56
	v_fmac_f32_e32 v87, v24, v24
	v_fmac_f32_e32 v88, v20, v20
	v_fmac_f32_e32 v85, v53, v53
	v_fmac_f32_e32 v86, v57, v57
	v_fmac_f32_e32 v87, v25, v25
	v_fmac_f32_e32 v88, v21, v21
	v_fmac_f32_e32 v85, v14, v14
	v_fmac_f32_e32 v86, v10, v10
	v_fmac_f32_e32 v87, v6, v6
	v_fmac_f32_e32 v88, v2, v2
	v_fmac_f32_e32 v85, v15, v15
	v_fmac_f32_e32 v86, v11, v11
	v_fmac_f32_e32 v87, v7, v7
	v_fmac_f32_e32 v88, v3, v3
	v_fmac_f32_e32 v85, v16, v16
	v_fmac_f32_e32 v86, v12, v12
	v_fmac_f32_e32 v87, v8, v8
	v_fmac_f32_e32 v88, v4, v4
	v_fmac_f32_e32 v85, v17, v17
	v_fmac_f32_e32 v86, v13, v13
	v_fmac_f32_e32 v87, v9, v9
	v_fmac_f32_e32 v88, v5, v5
	v_add_f32_e32 v85, v85, v86
	v_add_f32_e32 v87, v87, v88
	v_add_f32_e32 v38, v85, v87
	s_nop 1
	v_add_f32_dpp v38, v38, v38 row_shr:1 row_mask:0xf bank_mask:0xf bound_ctrl:1
	s_nop 1
	v_add_f32_dpp v38, v38, v38 row_shr:2 row_mask:0xf bank_mask:0xf bound_ctrl:1
	s_nop 1
	v_add_f32_dpp v38, v38, v38 row_shr:4 row_mask:0xf bank_mask:0xf bound_ctrl:1
	s_nop 1
	v_add_f32_dpp v38, v38, v38 row_shr:8 row_mask:0xf bank_mask:0xf bound_ctrl:1
	s_nop 1
	v_mov_b32_dpp v40, v38 row_bcast:15 row_mask:0xa bank_mask:0xf
	v_add_f32_e32 v38, v38, v40
	s_nop 1
	v_mov_b32_dpp v84, v38 row_bcast:31 row_mask:0xc bank_mask:0xf
	v_add_f32_e32 v38, v38, v84
	s_nop 0
	v_readlane_b32 s10, v38, 63
	s_nop 1
	v_fma_f32 v38, s10, v46, v45
	v_mul_f32_e32 v39, 0x4b800000, v38
	v_cmp_gt_f32_e32 vcc, s18, v38
	s_nop 1
	v_cndmask_b32_e32 v38, v38, v39, vcc
	v_rsq_f32_e32 v40, v38
	v_lshl_add_u64 v[38:39], v[36:37], 0, s[2:3]
	v_mul_f32_e32 v70, 0x45800000, v40
	v_cndmask_b32_e32 v40, v40, v70, vcc
	v_pk_mul_f32 v[50:51], v[50:51], v[40:41] op_sel_hi:[1,0]
	v_pk_mul_f32 v[52:53], v[52:53], v[40:41] op_sel_hi:[1,0]
	v_pk_mul_f32 v[54:55], v[54:55], v[40:41] op_sel_hi:[1,0]
	v_pk_mul_f32 v[56:57], v[56:57], v[40:41] op_sel_hi:[1,0]
	v_pk_mul_f32 v[22:23], v[22:23], v[40:41] op_sel_hi:[1,0]
	v_pk_mul_f32 v[24:25], v[24:25], v[40:41] op_sel_hi:[1,0]
	v_pk_mul_f32 v[18:19], v[18:19], v[40:41] op_sel_hi:[1,0]
	v_pk_mul_f32 v[20:21], v[20:21], v[40:41] op_sel_hi:[1,0]
	v_pk_mul_f32 v[14:15], v[14:15], v[40:41] op_sel_hi:[1,0]
	v_pk_mul_f32 v[16:17], v[16:17], v[40:41] op_sel_hi:[1,0]
	v_pk_mul_f32 v[10:11], v[10:11], v[40:41] op_sel_hi:[1,0]
	v_pk_mul_f32 v[12:13], v[12:13], v[40:41] op_sel_hi:[1,0]
	v_pk_mul_f32 v[6:7], v[6:7], v[40:41] op_sel_hi:[1,0]
	v_pk_mul_f32 v[8:9], v[8:9], v[40:41] op_sel_hi:[1,0]
	v_pk_mul_f32 v[2:3], v[2:3], v[40:41] op_sel_hi:[1,0]
	v_pk_mul_f32 v[4:5], v[4:5], v[40:41] op_sel_hi:[1,0]
	v_pk_mul_f32 v[50:51], v[90:91], v[50:51]
	v_pk_mul_f32 v[52:53], v[92:93], v[52:53]
	v_pk_mul_f32 v[54:55], v[94:95], v[54:55]
	v_pk_mul_f32 v[56:57], v[96:97], v[56:57]
	v_pk_mul_f32 v[22:23], v[98:99], v[22:23]
	v_pk_mul_f32 v[24:25], v[100:101], v[24:25]
	v_pk_mul_f32 v[18:19], v[102:103], v[18:19]
	v_pk_mul_f32 v[20:21], v[104:105], v[20:21]
	v_pk_mul_f32 v[14:15], v[106:107], v[14:15]
	v_pk_mul_f32 v[16:17], v[108:109], v[16:17]
	v_pk_mul_f32 v[10:11], v[110:111], v[10:11]
	v_pk_mul_f32 v[12:13], v[112:113], v[12:13]
	v_pk_mul_f32 v[6:7], v[114:115], v[6:7]
	v_pk_mul_f32 v[8:9], v[116:117], v[8:9]
	v_pk_mul_f32 v[2:3], v[118:119], v[2:3]
	v_pk_mul_f32 v[4:5], v[120:121], v[4:5]
	s_cmp_lg_u32 s28, 0
	s_cbranch_scc0 .Lp1_mod_a
	s_cmp_lg_u32 s21, 0
	s_cbranch_scc1 .Lp1_w8_a
	s_waitcnt vmcnt(0)
	s_branch .Lp1_one_a

; __device__ __forceinline__ unsigned pk2(float lo, float hi) { return f2bf(lo) | (f2bf(hi) << 16); }
; __device__ __forceinline__ void phase1(const Args& a, int lane, int wave, int vcu, int G) {
;     ...
;         const float* xr = m < NT ? a.in[0] + (size_t)m * 2048 : a.in[2] + (size_t)(m - NT) * 2048;
;         const float* mr = mod + (size_t)(m < NT ? (m >> 11) : 8) * 12288;
;         f32x4 v[8]; float ss = 0.f;
; #pragma unroll
;         for (int j = 0; j < 8; ++j) { v[j] = __builtin_nontemporal_load((const f32x4*)(xr + 4 * (lane + 64 * j))); ss += v[j][0] * v[j][0] + v[j][1] * v[j][1] + v[j][2] * v[j][2] + v[j][3] * v[j][3]; }
;     ...
;         for (int j = 0; j < 8; ++j) { const int c = 4 * (lane + 64 * j); const f32x4 gg = *(const f32x4*)(g + c), sh = *(const f32x4*)(mr + c), sc = *(const f32x4*)(mr + 2048 + c);
;             const f32x4 o = v[j] * rstd * gg * (sc + 1.f) + sh;
;             v2u q; q.x = pk2(o[0], o[1]); q.y = pk2(o[2], o[3]); *(v2u*)(H + (size_t)m * 2048 + c) = q; }
.Lp1_one_a:
	v_pk_add_f32 v[122:123], v[122:123], 1.0 op_sel_hi:[1,0]
	v_pk_add_f32 v[124:125], v[124:125], 1.0 op_sel_hi:[1,0]
	v_pk_add_f32 v[126:127], v[126:127], 1.0 op_sel_hi:[1,0]
	v_pk_add_f32 v[128:129], v[128:129], 1.0 op_sel_hi:[1,0]
	v_pk_add_f32 v[130:131], v[130:131], 1.0 op_sel_hi:[1,0]
	v_pk_add_f32 v[132:133], v[132:133], 1.0 op_sel_hi:[1,0]
	v_pk_add_f32 v[134:135], v[134:135], 1.0 op_sel_hi:[1,0]
	v_pk_add_f32 v[136:137], v[136:137], 1.0 op_sel_hi:[1,0]
	v_pk_add_f32 v[138:139], v[138:139], 1.0 op_sel_hi:[1,0]
	v_pk_add_f32 v[140:141], v[140:141], 1.0 op_sel_hi:[1,0]
	v_pk_add_f32 v[142:143], v[142:143], 1.0 op_sel_hi:[1,0]
	v_pk_add_f32 v[144:145], v[144:145], 1.0 op_sel_hi:[1,0]
	v_pk_add_f32 v[146:147], v[146:147], 1.0 op_sel_hi:[1,0]
	v_pk_add_f32 v[148:149], v[148:149], 1.0 op_sel_hi:[1,0]
	v_pk_add_f32 v[150:151], v[150:151], 1.0 op_sel_hi:[1,0]
	v_pk_add_f32 v[152:153], v[152:153], 1.0 op_sel_hi:[1,0]
.Lp1_mod_a:
	v_pk_fma_f32 v[50:51], v[122:123], v[50:51], v[154:155]
	v_pk_fma_f32 v[52:53], v[124:125], v[52:53], v[156:157]
	v_cvt_pk_bf16_f32 v50, v50, v51
	v_cvt_pk_bf16_f32 v51, v52, v53
	global_store_dwordx2 v[38:39], v[50:51], off
	v_pk_fma_f32 v[54:55], v[126:127], v[54:55], v[158:159]
	v_pk_fma_f32 v[56:57], v[128:129], v[56:57], v[160:161]
	v_cvt_pk_bf16_f32 v54, v54, v55
	v_cvt_pk_bf16_f32 v55, v56, v57
	global_store_dwordx2 v[38:39], v[54:55], off offset:512
	v_pk_fma_f32 v[22:23], v[130:131], v[22:23], v[162:163]
	v_pk_fma_f32 v[24:25], v[132:133], v[24:25], v[164:165]
	v_cvt_pk_bf16_f32 v22, v22, v23
	v_cvt_pk_bf16_f32 v23, v24, v25
	global_store_dwordx2 v[38:39], v[22:23], off offset:1024
	v_pk_fma_f32 v[18:19], v[134:135], v[18:19], v[166:167]
	v_pk_fma_f32 v[20:21], v[136:137], v[20:21], v[168:169]
	v_cvt_pk_bf16_f32 v18, v18, v19
	v_cvt_pk_bf16_f32 v19, v20, v21
	global_store_dwordx2 v[38:39], v[18:19], off offset:1536
	v_pk_fma_f32 v[14:15], v[138:139], v[14:15], v[170:171]
	v_pk_fma_f32 v[16:17], v[140:141], v[16:17], v[172:173]
	v_cvt_pk_bf16_f32 v14, v14, v15
	v_cvt_pk_bf16_f32 v15, v16, v17
	global_store_dwordx2 v[38:39], v[14:15], off offset:2048
	v_pk_fma_f32 v[10:11], v[142:143], v[10:11], v[174:175]
	v_pk_fma_f32 v[12:13], v[144:145], v[12:13], v[176:177]
	v_cvt_pk_bf16_f32 v10, v10, v11
	v_cvt_pk_bf16_f32 v11, v12, v13
	global_store_dwordx2 v[38:39], v[10:11], off offset:2560
	v_pk_fma_f32 v[6:7], v[146:147], v[6:7], v[178:179]
	v_pk_fma_f32 v[8:9], v[148:149], v[8:9], v[180:181]
	v_cvt_pk_bf16_f32 v6, v6, v7
	v_cvt_pk_bf16_f32 v7, v8, v9
	global_store_dwordx2 v[38:39], v[6:7], off offset:3072
	v_pk_fma_f32 v[2:3], v[150:151], v[2:3], v[182:183]
	v_pk_fma_f32 v[4:5], v[152:153], v[4:5], v[184:185]
	v_cvt_pk_bf16_f32 v2, v2, v3
	v_cvt_pk_bf16_f32 v3, v4, v5
	global_store_dwordx2 v[38:39], v[2:3], off offset:3584
	s_cmp_lg_u32 s21, 0
	s_cbranch_scc0 .LBB0_93
	s_min_i32 s10, s4, 0x4000
	s_ashr_i32 s10, s10, 11
	s_cmp_lg_u32 s10, s23
	s_cselect_b32 s28, 1, 0
	s_mov_b32 s23, s10
	s_cbranch_scc0 .Lp1_nomod_b
	s_mul_hi_i32 s13, s10, 0xc000
	s_mul_i32 s10, s10, 0xc000
	s_add_u32 s12, s16, s10
	s_addc_u32 s13, s17, s13
	s_add_u32 s14, s12, 0x2000
	s_addc_u32 s15, s13, 0
	global_load_dwordx4 v[122:125], v1, s[14:15]
	global_load_dwordx4 v[126:129], v1, s[14:15] offset:1024
	global_load_dwordx4 v[130:133], v1, s[14:15] offset:2048
	global_load_dwordx4 v[134:137], v1, s[14:15] offset:3072
	global_load_dwordx4 v[138:141], v41, s[14:15]
	global_load_dwordx4 v[142:145], v42, s[14:15]
	global_load_dwordx4 v[146:149], v43, s[14:15]
	global_load_dwordx4 v[150:153], v44, s[14:15]
	global_load_dwordx4 v[154:157], v1, s[12:13]
	global_load_dwordx4 v[158:161], v1, s[12:13] offset:1024
	global_load_dwordx4 v[162:165], v1, s[12:13] offset:2048
	global_load_dwordx4 v[166:169], v1, s[12:13] offset:3072
	global_load_dwordx4 v[170:173], v41, s[12:13]
	global_load_dwordx4 v[174:177], v42, s[12:13]
	global_load_dwordx4 v[178:181], v43, s[12:13]
	global_load_dwordx4 v[182:185], v44, s[12:13]

; __device__ __forceinline__ void phase1(const Args& a, int lane, int wave, int vcu, int G) {
;     ...
;         for (int j = 0; j < 8; ++j) { v[j] = __builtin_nontemporal_load((const f32x4*)(xr + 4 * (lane + 64 * j))); ss += v[j][0] * v[j][0] + v[j][1] * v[j][1] + v[j][2] * v[j][2] + v[j][3] * v[j][3]; }
;         const float rstd = rsqrtf(wave_sum(ss) * (1.f / 2048.f) + EPS);
; #pragma unroll
;         for (int j = 0; j < 8; ++j) { const int c = 4 * (lane + 64 * j); const f32x4 gg = *(const f32x4*)(g + c), sh = *(const f32x4*)(mr + c), sc = *(const f32x4*)(mr + 2048 + c);
;             const f32x4 o = v[j] * rstd * gg * (sc + 1.f) + sh;
.Lp1_red_b:
	v_mul_f32_e32 v85, v186, v186
	v_mul_f32_e32 v86, v190, v190
	v_mul_f32_e32 v87, v194, v194
	v_mul_f32_e32 v88, v198, v198
	v_fmac_f32_e32 v85, v187, v187
	v_fmac_f32_e32 v86, v191, v191
	v_fmac_f32_e32 v87, v195, v195
	v_fmac_f32_e32 v88, v199, v199
	v_fmac_f32_e32 v85, v188, v188
	v_fmac_f32_e32 v86, v192, v192
	v_fmac_f32_e32 v87, v196, v196
	v_fmac_f32_e32 v88, v200, v200
	v_fmac_f32_e32 v85, v189, v189
	v_fmac_f32_e32 v86, v193, v193
	v_fmac_f32_e32 v87, v197, v197
	v_fmac_f32_e32 v88, v201, v201
	v_fmac_f32_e32 v85, v202, v202
	v_fmac_f32_e32 v86, v206, v206
	v_fmac_f32_e32 v87, v210, v210
	v_fmac_f32_e32 v88, v214, v214
	v_fmac_f32_e32 v85, v203, v203
	v_fmac_f32_e32 v86, v207, v207
	v_fmac_f32_e32 v87, v211, v211
	v_fmac_f32_e32 v88, v215, v215
	v_fmac_f32_e32 v85, v204, v204
	v_fmac_f32_e32 v86, v208, v208
	v_fmac_f32_e32 v87, v212, v212
	v_fmac_f32_e32 v88, v216, v216
	v_fmac_f32_e32 v85, v205, v205
	v_fmac_f32_e32 v86, v209, v209
	v_fmac_f32_e32 v87, v213, v213
	v_fmac_f32_e32 v88, v217, v217
	v_add_f32_e32 v85, v85, v86
	v_add_f32_e32 v87, v87, v88
	v_add_f32_e32 v38, v85, v87
	s_nop 1
	v_add_f32_dpp v38, v38, v38 row_shr:1 row_mask:0xf bank_mask:0xf bound_ctrl:1
	s_nop 1
	v_add_f32_dpp v38, v38, v38 row_shr:2 row_mask:0xf bank_mask:0xf bound_ctrl:1
	s_nop 1
	v_add_f32_dpp v38, v38, v38 row_shr:4 row_mask:0xf bank_mask:0xf bound_ctrl:1
	s_nop 1
	v_add_f32_dpp v38, v38, v38 row_shr:8 row_mask:0xf bank_mask:0xf bound_ctrl:1
	s_nop 1
	v_mov_b32_dpp v40, v38 row_bcast:15 row_mask:0xa bank_mask:0xf
	v_add_f32_e32 v38, v38, v40
	s_nop 1
	v_mov_b32_dpp v84, v38 row_bcast:31 row_mask:0xc bank_mask:0xf
	v_add_f32_e32 v38, v38, v84
	s_nop 0
	v_readlane_b32 s10, v38, 63
	s_nop 1
	v_fma_f32 v38, s10, v46, v45
	v_mul_f32_e32 v39, 0x4b800000, v38
	v_cmp_gt_f32_e32 vcc, s18, v38
	s_nop 1
	v_cndmask_b32_e32 v38, v38, v39, vcc
	v_rsq_f32_e32 v40, v38
	v_lshl_add_u64 v[38:39], v[36:37], 0, s[2:3]
	v_mul_f32_e32 v70, 0x45800000, v40
	v_cndmask_b32_e32 v40, v40, v70, vcc
	v_pk_mul_f32 v[186:187], v[186:187], v[40:41] op_sel_hi:[1,0]
	v_pk_mul_f32 v[188:189], v[188:189], v[40:41] op_sel_hi:[1,0]
	v_pk_mul_f32 v[190:191], v[190:191], v[40:41] op_sel_hi:[1,0]
	v_pk_mul_f32 v[192:193], v[192:193], v[40:41] op_sel_hi:[1,0]
	v_pk_mul_f32 v[194:195], v[194:195], v[40:41] op_sel_hi:[1,0]
	v_pk_mul_f32 v[196:197], v[196:197], v[40:41] op_sel_hi:[1,0]
	v_pk_mul_f32 v[198:199], v[198:199], v[40:41] op_sel_hi:[1,0]
	v_pk_mul_f32 v[200:201], v[200:201], v[40:41] op_sel_hi:[1,0]
	v_pk_mul_f32 v[202:203], v[202:203], v[40:41] op_sel_hi:[1,0]
	v_pk_mul_f32 v[204:205], v[204:205], v[40:41] op_sel_hi:[1,0]
	v_pk_mul_f32 v[206:207], v[206:207], v[40:41] op_sel_hi:[1,0]
	v_pk_mul_f32 v[208:209], v[208:209], v[40:41] op_sel_hi:[1,0]
	v_pk_mul_f32 v[210:211], v[210:211], v[40:41] op_sel_hi:[1,0]
	v_pk_mul_f32 v[212:213], v[212:213], v[40:41] op_sel_hi:[1,0]
	v_pk_mul_f32 v[214:215], v[214:215], v[40:41] op_sel_hi:[1,0]
	v_pk_mul_f32 v[216:217], v[216:217], v[40:41] op_sel_hi:[1,0]
	v_pk_mul_f32 v[186:187], v[90:91], v[186:187]
	v_pk_mul_f32 v[188:189], v[92:93], v[188:189]
	v_pk_mul_f32 v[190:191], v[94:95], v[190:191]
	v_pk_mul_f32 v[192:193], v[96:97], v[192:193]
	v_pk_mul_f32 v[194:195], v[98:99], v[194:195]
	v_pk_mul_f32 v[196:197], v[100:101], v[196:197]
	v_pk_mul_f32 v[198:199], v[102:103], v[198:199]
	v_pk_mul_f32 v[200:201], v[104:105], v[200:201]
	v_pk_mul_f32 v[202:203], v[106:107], v[202:203]
	v_pk_mul_f32 v[204:205], v[108:109], v[204:205]
	v_pk_mul_f32 v[206:207], v[110:111], v[206:207]
	v_pk_mul_f32 v[208:209], v[112:113], v[208:209]
	v_pk_mul_f32 v[210:211], v[114:115], v[210:211]
	v_pk_mul_f32 v[212:213], v[116:117], v[212:213]
	v_pk_mul_f32 v[214:215], v[118:119], v[214:215]
	v_pk_mul_f32 v[216:217], v[120:121], v[216:217]
	s_cmp_lg_u32 s28, 0
	s_cbranch_scc0 .Lp1_mod_b
	s_cmp_lg_u32 s21, 0
	s_cbranch_scc1 .Lp1_w8_b
	s_waitcnt vmcnt(0)
	s_branch .Lp1_one_b

; __device__ __forceinline__ unsigned pk2(float lo, float hi) { return f2bf(lo) | (f2bf(hi) << 16); }
; __device__ __forceinline__ void phase1(const Args& a, int lane, int wave, int vcu, int G) {
;     ...
;         for (int j = 0; j < 8; ++j) { const int c = 4 * (lane + 64 * j); const f32x4 gg = *(const f32x4*)(g + c), sh = *(const f32x4*)(mr + c), sc = *(const f32x4*)(mr + 2048 + c);
;             const f32x4 o = v[j] * rstd * gg * (sc + 1.f) + sh;
;             v2u q; q.x = pk2(o[0], o[1]); q.y = pk2(o[2], o[3]); *(v2u*)(H + (size_t)m * 2048 + c) = q; }
.Lp1_mod_b:
	v_pk_fma_f32 v[186:187], v[122:123], v[186:187], v[154:155]
	v_pk_fma_f32 v[188:189], v[124:125], v[188:189], v[156:157]
	v_cvt_pk_bf16_f32 v186, v186, v187
	v_cvt_pk_bf16_f32 v187, v188, v189
	global_store_dwordx2 v[38:39], v[186:187], off
	v_pk_fma_f32 v[190:191], v[126:127], v[190:191], v[158:159]
	v_pk_fma_f32 v[192:193], v[128:129], v[192:193], v[160:161]
	v_cvt_pk_bf16_f32 v190, v190, v191
	v_cvt_pk_bf16_f32 v191, v192, v193
	global_store_dwordx2 v[38:39], v[190:191], off offset:512
	v_pk_fma_f32 v[194:195], v[130:131], v[194:195], v[162:163]
	v_pk_fma_f32 v[196:197], v[132:133], v[196:197], v[164:165]
	v_cvt_pk_bf16_f32 v194, v194, v195
	v_cvt_pk_bf16_f32 v195, v196, v197
	global_store_dwordx2 v[38:39], v[194:195], off offset:1024
	v_pk_fma_f32 v[198:199], v[134:135], v[198:199], v[166:167]
	v_pk_fma_f32 v[200:201], v[136:137], v[200:201], v[168:169]
	v_cvt_pk_bf16_f32 v198, v198, v199
	v_cvt_pk_bf16_f32 v199, v200, v201
	global_store_dwordx2 v[38:39], v[198:199], off offset:1536
	v_pk_fma_f32 v[202:203], v[138:139], v[202:203], v[170:171]
	v_pk_fma_f32 v[204:205], v[140:141], v[204:205], v[172:173]
	v_cvt_pk_bf16_f32 v202, v202, v203
	v_cvt_pk_bf16_f32 v203, v204, v205
	global_store_dwordx2 v[38:39], v[202:203], off offset:2048
	v_pk_fma_f32 v[206:207], v[142:143], v[206:207], v[174:175]
	v_pk_fma_f32 v[208:209], v[144:145], v[208:209], v[176:177]
	v_cvt_pk_bf16_f32 v206, v206, v207
	v_cvt_pk_bf16_f32 v207, v208, v209
	global_store_dwordx2 v[38:39], v[206:207], off offset:2560
	v_pk_fma_f32 v[210:211], v[146:147], v[210:211], v[178:179]
	v_pk_fma_f32 v[212:213], v[148:149], v[212:213], v[180:181]
	v_cvt_pk_bf16_f32 v210, v210, v211
	v_cvt_pk_bf16_f32 v211, v212, v213
	global_store_dwordx2 v[38:39], v[210:211], off offset:3072
	v_pk_fma_f32 v[214:215], v[150:151], v[214:215], v[182:183]
	v_pk_fma_f32 v[216:217], v[152:153], v[216:217], v[184:185]
	v_cvt_pk_bf16_f32 v214, v214, v215
	v_cvt_pk_bf16_f32 v215, v216, v217
	global_store_dwordx2 v[38:39], v[214:215], off offset:3584
	s_cmp_lg_u32 s21, 0
	s_cbranch_scc0 .LBB0_93
	s_branch .Lp1_top
